# baseline (speedup 1.0000x reference)
_Z13logits_kernelPKDv8_DF16bS1_PKfS3_PDv2_fS5_Pf:
	s_load_dwordx4 s[4:7], s[0:1], 0x0
	s_load_dwordx4 s[12:15], s[0:1], 0x10
	s_load_dwordx4 s[24:27], s[0:1], 0x20
	s_load_dwordx2 s[28:29], s[0:1], 0x30
	s_and_b32 s3, s2, 1
	s_lshl_b32 s3, s3, 3
	s_bfe_u32 s10, s2, 0x30003
	s_or_b32 s10, s10, s3
	s_bfe_u32 s3, s2, 0x20001
	s_lshl_b32 s3, s3, 2
	s_lshr_b32 s8, s2, 6
	s_or_b32 s3, s3, s8
	v_lshrrev_b32_e32 v1, 6, v0
	v_and_b32_e32 v2, 63, v0
	s_movk_i32 s11, 0x3000
	v_lshlrev_b32_e32 v2, 4, v2
	v_and_b32_e32 v5, 31, v0
	v_mad_u32_u24 v2, v1, s11, v2
	v_lshlrev_b32_e32 v5, 2, v5
	s_lshl_b32 s9, s3, 9
	v_add_u32_e32 v3, 0x1000, v2
	v_add_u32_e32 v4, 0x2000, v2
	v_add_u32_e32 v5, s9, v5
	s_mul_i32 s8, s10, 0xc000
	s_mul_i32 s9, s3, 0x30000
	s_waitcnt lgkmcnt(0)
	s_load_dword s22, s[14:15], 0x0
	v_readfirstlane_b32 s23, v0
	s_nop 0
	s_cmp_lg_u32 s23, 0
	s_cbranch_scc1 .Llg_nocnt
	global_load_dword v248, v5, s[12:13]
	global_load_dword v249, v5, s[12:13] offset:128
	global_load_dword v250, v5, s[12:13] offset:256
	global_load_dword v251, v5, s[12:13] offset:384
.Llg_nocnt:
	s_add_u32 s4, s4, s8
	s_addc_u32 s5, s5, 0
	s_add_u32 s6, s6, s9
	s_addc_u32 s7, s7, 0
	s_add_u32 s16, s6, 0xc000
	s_addc_u32 s17, s7, 0
	s_add_u32 s18, s6, 0x18000
	s_addc_u32 s19, s7, 0
	s_add_u32 s20, s6, 0x24000
	s_addc_u32 s21, s7, 0
	global_load_dwordx4 v[8:11], v2, s[4:5]
	global_load_dwordx4 v[56:59], v2, s[6:7]
	global_load_dwordx4 v[104:107], v2, s[16:17]
	global_load_dwordx4 v[152:155], v2, s[18:19]
	global_load_dwordx4 v[200:203], v2, s[20:21]
	global_load_dwordx4 v[12:15], v2, s[4:5] offset:1024
	global_load_dwordx4 v[60:63], v2, s[6:7] offset:1024
	global_load_dwordx4 v[108:111], v2, s[16:17] offset:1024
	global_load_dwordx4 v[156:159], v2, s[18:19] offset:1024
	global_load_dwordx4 v[204:207], v2, s[20:21] offset:1024
	global_load_dwordx4 v[16:19], v2, s[4:5] offset:2048
	global_load_dwordx4 v[64:67], v2, s[6:7] offset:2048
	global_load_dwordx4 v[112:115], v2, s[16:17] offset:2048
	global_load_dwordx4 v[160:163], v2, s[18:19] offset:2048
	global_load_dwordx4 v[208:211], v2, s[20:21] offset:2048
	global_load_dwordx4 v[20:23], v2, s[4:5] offset:3072
	global_load_dwordx4 v[68:71], v2, s[6:7] offset:3072
	global_load_dwordx4 v[116:119], v2, s[16:17] offset:3072
	global_load_dwordx4 v[164:167], v2, s[18:19] offset:3072
	global_load_dwordx4 v[212:215], v2, s[20:21] offset:3072
	global_load_dwordx4 v[24:27], v3, s[4:5]
	global_load_dwordx4 v[72:75], v3, s[6:7]
	global_load_dwordx4 v[120:123], v3, s[16:17]
	global_load_dwordx4 v[168:171], v3, s[18:19]
	global_load_dwordx4 v[216:219], v3, s[20:21]
	global_load_dwordx4 v[28:31], v3, s[4:5] offset:1024
	global_load_dwordx4 v[76:79], v3, s[6:7] offset:1024
	global_load_dwordx4 v[124:127], v3, s[16:17] offset:1024
	global_load_dwordx4 v[172:175], v3, s[18:19] offset:1024
	global_load_dwordx4 v[220:223], v3, s[20:21] offset:1024
	global_load_dwordx4 v[32:35], v3, s[4:5] offset:2048
	global_load_dwordx4 v[80:83], v3, s[6:7] offset:2048
	global_load_dwordx4 v[128:131], v3, s[16:17] offset:2048
	global_load_dwordx4 v[176:179], v3, s[18:19] offset:2048
	global_load_dwordx4 v[224:227], v3, s[20:21] offset:2048
	global_load_dwordx4 v[36:39], v3, s[4:5] offset:3072
	global_load_dwordx4 v[84:87], v3, s[6:7] offset:3072
	global_load_dwordx4 v[132:135], v3, s[16:17] offset:3072
	global_load_dwordx4 v[180:183], v3, s[18:19] offset:3072
	global_load_dwordx4 v[228:231], v3, s[20:21] offset:3072
	global_load_dwordx4 v[40:43], v4, s[4:5]
	global_load_dwordx4 v[88:91], v4, s[6:7]
	global_load_dwordx4 v[136:139], v4, s[16:17]
	global_load_dwordx4 v[184:187], v4, s[18:19]
	global_load_dwordx4 v[232:235], v4, s[20:21]
	global_load_dwordx4 v[44:47], v4, s[4:5] offset:1024
	global_load_dwordx4 v[92:95], v4, s[6:7] offset:1024
	global_load_dwordx4 v[140:143], v4, s[16:17] offset:1024
	global_load_dwordx4 v[188:191], v4, s[18:19] offset:1024
	global_load_dwordx4 v[236:239], v4, s[20:21] offset:1024
	global_load_dwordx4 v[48:51], v4, s[4:5] offset:2048
	global_load_dwordx4 v[96:99], v4, s[6:7] offset:2048
	global_load_dwordx4 v[144:147], v4, s[16:17] offset:2048
	global_load_dwordx4 v[192:195], v4, s[18:19] offset:2048
	global_load_dwordx4 v[240:243], v4, s[20:21] offset:2048
	global_load_dwordx4 v[52:55], v4, s[4:5] offset:3072
	global_load_dwordx4 v[100:103], v4, s[6:7] offset:3072
	global_load_dwordx4 v[148:151], v4, s[16:17] offset:3072
	global_load_dwordx4 v[196:199], v4, s[18:19] offset:3072
	global_load_dwordx4 v[244:247], v4, s[20:21] offset:3072
	s_waitcnt vmcnt(58)
	v_mfma_f32_32x32x16_bf16 a[0:15], v[8:11], v[56:59], 0
	s_waitcnt vmcnt(57)
	v_mfma_f32_32x32x16_bf16 a[0:15], v[8:11], v[104:107], a[0:15]
	s_waitcnt vmcnt(56)
	v_mfma_f32_32x32x16_bf16 a[0:15], v[8:11], v[152:155], a[0:15]
	s_waitcnt vmcnt(55)
	v_mfma_f32_32x32x16_bf16 a[0:15], v[8:11], v[200:203], a[0:15]
	s_waitcnt vmcnt(53)
	v_mfma_f32_32x32x16_bf16 a[0:15], v[12:15], v[60:63], a[0:15]
	s_waitcnt vmcnt(52)
	v_mfma_f32_32x32x16_bf16 a[0:15], v[12:15], v[108:111], a[0:15]
	s_waitcnt vmcnt(51)
	v_mfma_f32_32x32x16_bf16 a[0:15], v[12:15], v[156:159], a[0:15]
	s_waitcnt vmcnt(50)
	v_mfma_f32_32x32x16_bf16 a[0:15], v[12:15], v[204:207], a[0:15]
	s_waitcnt vmcnt(48)
	v_mfma_f32_32x32x16_bf16 a[0:15], v[16:19], v[64:67], a[0:15]
	s_waitcnt vmcnt(47)
	v_mfma_f32_32x32x16_bf16 a[0:15], v[16:19], v[112:115], a[0:15]
	s_waitcnt vmcnt(46)
	v_mfma_f32_32x32x16_bf16 a[0:15], v[16:19], v[160:163], a[0:15]
	s_waitcnt vmcnt(45)
	v_mfma_f32_32x32x16_bf16 a[0:15], v[16:19], v[208:211], a[0:15]
	s_waitcnt vmcnt(43)
	v_mfma_f32_32x32x16_bf16 a[0:15], v[20:23], v[68:71], a[0:15]
	s_waitcnt vmcnt(42)
	v_mfma_f32_32x32x16_bf16 a[0:15], v[20:23], v[116:119], a[0:15]
	s_waitcnt vmcnt(41)
	v_mfma_f32_32x32x16_bf16 a[0:15], v[20:23], v[164:167], a[0:15]
	s_waitcnt vmcnt(40)
	v_mfma_f32_32x32x16_bf16 a[0:15], v[20:23], v[212:215], a[0:15]
	s_waitcnt vmcnt(38)
	v_mfma_f32_32x32x16_bf16 a[0:15], v[24:27], v[72:75], a[0:15]
	s_waitcnt vmcnt(37)
	v_mfma_f32_32x32x16_bf16 a[0:15], v[24:27], v[120:123], a[0:15]
	s_waitcnt vmcnt(36)
	v_mfma_f32_32x32x16_bf16 a[0:15], v[24:27], v[168:171], a[0:15]
	s_waitcnt vmcnt(35)
	v_mfma_f32_32x32x16_bf16 a[0:15], v[24:27], v[216:219], a[0:15]
	s_waitcnt vmcnt(33)
	v_mfma_f32_32x32x16_bf16 a[0:15], v[28:31], v[76:79], a[0:15]
	s_waitcnt vmcnt(32)
	v_mfma_f32_32x32x16_bf16 a[0:15], v[28:31], v[124:127], a[0:15]
	s_waitcnt vmcnt(31)
	v_mfma_f32_32x32x16_bf16 a[0:15], v[28:31], v[172:175], a[0:15]
	s_waitcnt vmcnt(30)
	v_mfma_f32_32x32x16_bf16 a[0:15], v[28:31], v[220:223], a[0:15]
	s_waitcnt vmcnt(28)
	v_mfma_f32_32x32x16_bf16 a[0:15], v[32:35], v[80:83], a[0:15]
	s_waitcnt vmcnt(27)
	v_mfma_f32_32x32x16_bf16 a[0:15], v[32:35], v[128:131], a[0:15]
	s_waitcnt vmcnt(26)
	v_mfma_f32_32x32x16_bf16 a[0:15], v[32:35], v[176:179], a[0:15]
	s_waitcnt vmcnt(25)
	v_mfma_f32_32x32x16_bf16 a[0:15], v[32:35], v[224:227], a[0:15]
	s_waitcnt vmcnt(23)
	v_mfma_f32_32x32x16_bf16 a[0:15], v[36:39], v[84:87], a[0:15]
	s_waitcnt vmcnt(22)
	v_mfma_f32_32x32x16_bf16 a[0:15], v[36:39], v[132:135], a[0:15]
	s_waitcnt vmcnt(21)
	v_mfma_f32_32x32x16_bf16 a[0:15], v[36:39], v[180:183], a[0:15]
	s_waitcnt vmcnt(20)
	v_mfma_f32_32x32x16_bf16 a[0:15], v[36:39], v[228:231], a[0:15]
	s_waitcnt vmcnt(18)
	v_mfma_f32_32x32x16_bf16 a[0:15], v[40:43], v[88:91], a[0:15]
	s_waitcnt vmcnt(17)
	v_mfma_f32_32x32x16_bf16 a[0:15], v[40:43], v[136:139], a[0:15]
	s_waitcnt vmcnt(16)
	v_mfma_f32_32x32x16_bf16 a[0:15], v[40:43], v[184:187], a[0:15]
	s_waitcnt vmcnt(15)
	v_mfma_f32_32x32x16_bf16 a[0:15], v[40:43], v[232:235], a[0:15]
	s_waitcnt vmcnt(13)
	v_mfma_f32_32x32x16_bf16 a[0:15], v[44:47], v[92:95], a[0:15]
	s_waitcnt vmcnt(12)
	v_mfma_f32_32x32x16_bf16 a[0:15], v[44:47], v[140:143], a[0:15]
	s_waitcnt vmcnt(11)
	v_mfma_f32_32x32x16_bf16 a[0:15], v[44:47], v[188:191], a[0:15]
	s_waitcnt vmcnt(10)
	v_mfma_f32_32x32x16_bf16 a[0:15], v[44:47], v[236:239], a[0:15]
	v_add_f32_e32 v8, 0, v248
	v_add_f32_e32 v8, v8, v249
	v_add_f32_e32 v8, v8, v250
	v_add_f32_e32 v8, v8, v251
	v_mov_b32_e32 v9, 0x3fb8aa3b
	s_waitcnt lgkmcnt(0)
	v_mul_f32_e32 v9, s22, v9
	v_exp_f32_e32 v9, v9
	v_add_f32_e32 v10, 0x2b8cbccc, v8
	v_div_scale_f32 v11, s[8:9], v10, v10, v9
	v_rcp_f32_e32 v12, v11
	v_div_scale_f32 v13, vcc, v9, v10, v9
	v_fma_f32 v14, -v11, v12, 1.0
	v_fmac_f32_e32 v12, v14, v12
	v_mul_f32_e32 v14, v13, v12
	v_fma_f32 v15, -v11, v14, v13
	v_fmac_f32_e32 v14, v15, v12
	v_fma_f32 v11, -v11, v14, v13
	v_div_fmas_f32 v11, v11, v12, v14
	v_div_fixup_f32 v9, v11, v10, v9
	v_lshlrev_b32_e32 v10, 2, v0
	v_add_u32_e32 v10, 0x4000, v10
	v_cmp_gt_u32_e32 vcc, 32, v0
	s_and_saveexec_b64 s[8:9], vcc
	ds_write2_b32 v10, v8, v9 offset0:128 offset1:160
	s_mov_b64 exec, s[8:9]
	s_waitcnt vmcnt(8)
	v_mfma_f32_32x32x16_bf16 a[0:15], v[48:51], v[96:99], a[0:15]
	s_waitcnt vmcnt(7)
	v_mfma_f32_32x32x16_bf16 a[0:15], v[48:51], v[144:147], a[0:15]
	s_waitcnt vmcnt(6)
	v_mfma_f32_32x32x16_bf16 a[0:15], v[48:51], v[192:195], a[0:15]
	s_waitcnt vmcnt(5)
	v_mfma_f32_32x32x16_bf16 a[0:15], v[48:51], v[240:243], a[0:15]
	v_mul_u32_u24_e32 v1, 0x1080, v1
	s_movk_i32 s4, 0x7f
	s_movk_i32 s6, 0x84
	v_cmp_lt_u32_e32 vcc, s4, v0
	v_lshrrev_b32_e32 v11, 3, v0
	v_and_b32_e32 v10, 31, v0
	v_and_b32_e32 v11, 4, v11
	v_mul_u32_u24_e32 v11, 0x84, v11
	v_lshlrev_b32_e32 v9, 2, v10
	v_bfe_u32 v6, v0, 2, 5
	v_and_b32_e32 v7, 3, v0
	v_add3_u32 v1, v1, v11, v9
	v_lshlrev_b32_e32 v8, 3, v7
	s_waitcnt vmcnt(3)
	v_mfma_f32_32x32x16_bf16 a[0:15], v[52:55], v[100:103], a[0:15]
	s_waitcnt vmcnt(2)
	v_mfma_f32_32x32x16_bf16 a[0:15], v[52:55], v[148:151], a[0:15]
	s_waitcnt vmcnt(1)
	v_mfma_f32_32x32x16_bf16 a[0:15], v[52:55], v[196:199], a[0:15]
	s_waitcnt vmcnt(0)
	v_mfma_f32_32x32x16_bf16 a[0:15], v[52:55], v[244:247], a[0:15]
	s_nop 11
	ds_write_b32 v1, a0
	ds_write_b32 v1, a1 offset:132
	ds_write_b32 v1, a2 offset:264
	ds_write_b32 v1, a3 offset:396
	ds_write_b32 v1, a4 offset:1056
	ds_write_b32 v1, a5 offset:1188
	ds_write_b32 v1, a6 offset:1320
	ds_write_b32 v1, a7 offset:1452
	ds_write_b32 v1, a8 offset:2112
	ds_write_b32 v1, a9 offset:2244
	ds_write_b32 v1, a10 offset:2376
	ds_write_b32 v1, a11 offset:2508
	ds_write_b32 v1, a12 offset:3168
	ds_write_b32 v1, a13 offset:3300
	ds_write_b32 v1, a14 offset:3432
	ds_write_b32 v1, a15 offset:3564
	v_bfe_u32 v6, v0, 2, 5
	v_and_b32_e32 v7, 3, v0
	v_lshlrev_b32_e32 v9, 3, v7
	v_readfirstlane_b32 s30, v0
	v_sub_u32_e32 v10, v6, v9
	s_waitcnt lgkmcnt(0)
	s_barrier
	s_cmpk_ge_u32 s30, 0x80
	s_cbranch_scc1 .Llg_k1
	v_mul_u32_u24_e32 v2, 0x84, v6
	v_lshlrev_b32_e32 v8, 5, v7
	v_add_u32_e32 v2, v2, v8
	v_add_u32_e32 v8, 0x4280, v8
	v_add_u32_e32 v3, 0x1080, v2
	v_add_u32_e32 v4, 0x2100, v2
	v_add_u32_e32 v5, 0x3180, v2
	ds_read_b128 v[48:51], v8
	ds_read_b128 v[52:55], v8 offset:16
	ds_read2_b32 v[16:17], v2 offset0:0 offset1:1
	ds_read2_b32 v[18:19], v2 offset0:2 offset1:3
	ds_read2_b32 v[20:21], v2 offset0:4 offset1:5
	ds_read2_b32 v[22:23], v2 offset0:6 offset1:7
	ds_read2_b32 v[24:25], v3 offset0:0 offset1:1
	ds_read2_b32 v[26:27], v3 offset0:2 offset1:3
	ds_read2_b32 v[28:29], v3 offset0:4 offset1:5
	ds_read2_b32 v[30:31], v3 offset0:6 offset1:7
	ds_read2_b32 v[32:33], v4 offset0:0 offset1:1
	ds_read2_b32 v[34:35], v4 offset0:2 offset1:3
	ds_read2_b32 v[36:37], v4 offset0:4 offset1:5
	ds_read2_b32 v[38:39], v4 offset0:6 offset1:7
	s_waitcnt lgkmcnt(4)
	ds_read2_b32 v[40:41], v5 offset0:0 offset1:1
	ds_read2_b32 v[42:43], v5 offset0:2 offset1:3
	ds_read2_b32 v[44:45], v5 offset0:4 offset1:5
	ds_read2_b32 v[46:47], v5 offset0:6 offset1:7
	s_waitcnt lgkmcnt(0)
	s_branch .Llg_join
